# v34 plus all individually-neutral structural changes (P2c order swap on odd WGs, DSA staging at top, one indexer barrier less, batched Gram reads, store-ack deferral, dead barrier release atomics remo
# speedup vs baseline: 1.0058x; 1.0018x over previous
.LBB0_117:
	s_or_b64 exec, exec, s[12:13]
	v_cvt_f32_u32_e32 v4, v1
	s_waitcnt vmcnt(0)
	v_readfirstlane_b32 s10, v3
	s_add_u32 s12, s86, 0x3500
	s_addc_u32 s13, s87, 0
	v_rcp_iflag_f32_e32 v4, v4
	v_add_u32_e32 v2, s10, v2
	v_add_u32_e32 v5, 1, v2
	s_mov_b64 s[14:15], 0
	v_mul_f32_e32 v3, 0x4f7ffffe, v4
	v_cvt_u32_f32_e32 v3, v3
	v_sub_u32_e32 v4, 0, v1
	v_mul_lo_u32 v4, v4, v3
	v_mul_hi_u32 v4, v3, v4
	v_add_u32_e32 v3, v3, v4
	v_mul_hi_u32 v3, v2, v3
	v_mul_lo_u32 v4, v3, v1
	v_sub_u32_e32 v2, v2, v4
	v_add_u32_e32 v6, 1, v3
	v_cmp_ge_u32_e32 vcc, v2, v1
	v_sub_u32_e32 v4, v2, v1
	s_nop 0
	v_cndmask_b32_e32 v3, v3, v6, vcc
	v_cndmask_b32_e32 v2, v2, v4, vcc
	v_add_u32_e32 v4, 1, v3
	v_cmp_ge_u32_e32 vcc, v2, v1
	s_nop 1
	v_cndmask_b32_e32 v4, v3, v4, vcc
	v_mul_lo_u32 v2, v1, v4
	v_add_u32_e32 v1, v2, v1
	v_cmp_ne_u32_e32 vcc, v5, v1
	v_mov_b64_e32 v[2:3], s[12:13]
	s_and_saveexec_b64 s[10:11], vcc
	s_cbranch_execz .LBB0_129
	v_mov_b32_e32 v4, v1
	v_mov_b32_e32 v1, 0
	global_load_dword v2, v1, s[12:13] offset:-256 sc1
	s_mov_b64 s[18:19], 0
	s_waitcnt vmcnt(0)
	v_cmp_lt_u32_e32 vcc, v2, v4
	s_and_saveexec_b64 s[16:17], vcc
	s_cbranch_execz .LBB0_128
	s_add_u32 s14, s86, 0x200
	s_addc_u32 s15, s87, 0
	s_mov_b32 s28, 1
	s_branch .LBB0_121

.LBB0_131:
	s_or_b64 exec, exec, s[10:11]
	s_mov_b64 s[10:11], exec
	v_mbcnt_lo_u32_b32 v1, s10, 0
	v_mbcnt_hi_u32_b32 v1, s11, v1
	v_cmp_eq_u32_e32 vcc, 0, v1
	s_waitcnt vmcnt(0)
	s_and_saveexec_b64 s[12:13], vcc
	s_cbranch_execz .LBB0_133
	s_bcnt1_i32_b64 s10, s[10:11]
	v_mov_b32_e32 v1, 0x2000
	v_mov_b32_e32 v2, s10
.LBB0_133:
	s_or_b64 exec, exec, s[12:13]
	s_waitcnt vmcnt(0)

.LBB0_210:
	s_or_b64 exec, exec, s[10:11]
	s_mov_b64 s[10:11], exec
	v_mbcnt_lo_u32_b32 v1, s10, 0
	v_mbcnt_hi_u32_b32 v1, s11, v1
	v_cmp_eq_u32_e32 vcc, 0, v1
	s_waitcnt vmcnt(0)
	s_and_saveexec_b64 s[12:13], vcc
	s_cbranch_execz .LBB0_212
	s_bcnt1_i32_b64 s10, s[10:11]
	v_mov_b32_e32 v1, 0x2000
	v_mov_b32_e32 v2, s10
.LBB0_212:
	s_or_b64 exec, exec, s[12:13]
	s_waitcnt vmcnt(0)

.LBB0_529:
	s_or_b64 exec, exec, s[10:11]
	s_mov_b64 s[10:11], exec
	v_mbcnt_lo_u32_b32 v1, s10, 0
	v_mbcnt_hi_u32_b32 v1, s11, v1
	v_cmp_eq_u32_e32 vcc, 0, v1
	s_waitcnt vmcnt(0)
	s_and_saveexec_b64 s[12:13], vcc
	s_cbranch_execz .LBB0_531
	s_bcnt1_i32_b64 s10, s[10:11]
	v_mov_b32_e32 v1, 0x2000
	v_mov_b32_e32 v2, s10
.LBB0_531:
	s_or_b64 exec, exec, s[12:13]
	s_waitcnt vmcnt(0)

.LBB0_1276:
	s_or_b64 exec, exec, s[8:9]
	v_cvt_f32_u32_e32 v4, v1
	s_waitcnt vmcnt(0)
	v_readfirstlane_b32 s3, v3
	s_add_u32 s8, s86, 0x3500
	s_addc_u32 s9, s87, 0
	v_rcp_iflag_f32_e32 v4, v4
	v_add_u32_e32 v2, s3, v2
	v_add_u32_e32 v5, 1, v2
	s_mov_b64 s[10:11], 0
	v_mul_f32_e32 v3, 0x4f7ffffe, v4
	v_cvt_u32_f32_e32 v3, v3
	v_sub_u32_e32 v4, 0, v1
	v_mul_lo_u32 v4, v4, v3
	v_mul_hi_u32 v4, v3, v4
	v_add_u32_e32 v3, v3, v4
	v_mul_hi_u32 v3, v2, v3
	v_mul_lo_u32 v4, v3, v1
	v_sub_u32_e32 v2, v2, v4
	v_add_u32_e32 v6, 1, v3
	v_cmp_ge_u32_e32 vcc, v2, v1
	v_sub_u32_e32 v4, v2, v1
	s_nop 0
	v_cndmask_b32_e32 v3, v3, v6, vcc
	v_cndmask_b32_e32 v2, v2, v4, vcc
	v_add_u32_e32 v4, 1, v3
	v_cmp_ge_u32_e32 vcc, v2, v1
	s_nop 1
	v_cndmask_b32_e32 v4, v3, v4, vcc
	v_mul_lo_u32 v2, v1, v4
	v_add_u32_e32 v1, v2, v1
	v_cmp_ne_u32_e32 vcc, v5, v1
	v_mov_b64_e32 v[2:3], s[8:9]
	s_and_saveexec_b64 s[6:7], vcc
	s_cbranch_execz .LBB0_1288
	v_mov_b32_e32 v4, v1
	v_mov_b32_e32 v1, 0
	global_load_dword v2, v1, s[8:9] offset:-256 sc1
	s_mov_b64 s[14:15], 0
	s_waitcnt vmcnt(0)
	v_cmp_lt_u32_e32 vcc, v2, v4
	s_and_saveexec_b64 s[12:13], vcc
	s_cbranch_execz .LBB0_1287
	s_add_u32 s10, s86, 0x200
	s_addc_u32 s11, s87, 0
	s_mov_b32 s3, 1
	s_branch .LBB0_1280

.LBB0_1290:
	s_or_b64 exec, exec, s[6:7]
	s_mov_b64 s[6:7], exec
	v_mbcnt_lo_u32_b32 v1, s6, 0
	v_mbcnt_hi_u32_b32 v1, s7, v1
	v_cmp_eq_u32_e32 vcc, 0, v1
	s_waitcnt vmcnt(0)
	s_and_saveexec_b64 s[8:9], vcc
	s_cbranch_execz .LBB0_1292
	s_bcnt1_i32_b64 s3, s[6:7]
	v_mov_b32_e32 v1, 0x2000
	v_mov_b32_e32 v2, s3
.LBB0_1292:
	s_or_b64 exec, exec, s[8:9]
	s_waitcnt vmcnt(0)

.LBB0_1423:
	s_or_b64 exec, exec, s[6:7]
	s_mov_b64 s[6:7], exec
	v_mbcnt_lo_u32_b32 v1, s6, 0
	v_mbcnt_hi_u32_b32 v1, s7, v1
	v_cmp_eq_u32_e32 vcc, 0, v1
	s_waitcnt vmcnt(0)
	s_and_saveexec_b64 s[8:9], vcc
	s_cbranch_execz .LBB0_1425
	s_bcnt1_i32_b64 s3, s[6:7]
	v_mov_b32_e32 v1, 0x2000
	v_mov_b32_e32 v2, s3
.LBB0_1425:
	s_or_b64 exec, exec, s[8:9]
	s_waitcnt vmcnt(0)
